# v7 + grid barrier: CU leaders poll the top-level generation word directly (no per-XCD release hop)
# speedup vs baseline: 1.0079x; 1.0048x over previous
.LBB0_291:
	s_or_b64 exec, exec, s[8:9]
	v_cvt_f32_u32_e32 v4, v2
	s_waitcnt vmcnt(0)
	v_readfirstlane_b32 s6, v3
	v_sub_u32_e32 v3, 0, v2
	v_rcp_iflag_f32_e32 v4, v4
	v_add_u32_e32 v5, s6, v1
	v_mul_f32_e32 v4, 0x4f7ffffe, v4
	v_cvt_u32_f32_e32 v4, v4
	v_mul_lo_u32 v1, v3, v4
	v_mul_hi_u32 v1, v4, v1
	v_add_u32_e32 v1, v4, v1
	v_mul_hi_u32 v1, v5, v1
	v_mul_lo_u32 v3, v1, v2
	v_sub_u32_e32 v3, v5, v3
	v_add_u32_e32 v4, 1, v1
	v_cmp_ge_u32_e32 vcc, v3, v2
	s_nop 1
	v_cndmask_b32_e32 v1, v1, v4, vcc
	v_sub_u32_e32 v4, v3, v2
	v_cndmask_b32_e32 v3, v3, v4, vcc
	v_add_u32_e32 v4, 1, v1
	v_cmp_ge_u32_e32 vcc, v3, v2
	v_add_u32_e32 v3, 1, v5
	s_nop 0
	v_cndmask_b32_e32 v1, v1, v4, vcc
	v_mul_lo_u32 v4, v2, v1
	v_add_u32_e32 v2, v4, v2
	v_cmp_ne_u32_e32 vcc, v3, v2
	s_and_saveexec_b64 s[6:7], vcc
	s_xor_b64 s[6:7], exec, s[6:7]
	s_cbranch_execz .LBB0_305
	s_waitcnt lgkmcnt(0)
	s_add_u32 s12, s66, 0x7500
	s_addc_u32 s13, s67, 0
	v_mov_b32_e32 v0, 0
	global_load_dword v0, v0, s[12:13] sc1
	s_waitcnt vmcnt(0)
	v_cmp_eq_u32_e32 vcc, v0, v1
	s_and_saveexec_b64 s[8:9], vcc
	s_cbranch_execz .LBB0_304
	s_add_u32 s10, s66, 0x4200
	s_addc_u32 s11, s67, 0
	s_mov_b32 s24, 1
	s_mov_b64 s[14:15], 0
	v_mov_b32_e32 v0, 0
	s_branch .LBB0_295

.LBB0_322:
	s_or_b64 exec, exec, s[6:7]
	s_mov_b64 s[6:7], exec
	v_mbcnt_lo_u32_b32 v0, s6, 0
	v_mbcnt_hi_u32_b32 v0, s7, v0
	v_cmp_eq_u32_e32 vcc, 0, v0
	s_waitcnt vmcnt(0)
	buffer_inv sc1
	s_and_saveexec_b64 s[8:9], vcc
	s_cbranch_execz .LBB0_324
	s_bcnt1_i32_b64 s6, s[6:7]
	v_mov_b32_e32 v0, 0x2000
	v_mov_b32_e32 v1, s6
.LBB0_324:
	s_or_b64 exec, exec, s[8:9]
	s_waitcnt vmcnt(0)

.LBB0_407:
	s_or_b64 exec, exec, s[6:7]
	s_mov_b64 s[6:7], exec
	v_mbcnt_lo_u32_b32 v0, s6, 0
	v_mbcnt_hi_u32_b32 v0, s7, v0
	v_cmp_eq_u32_e32 vcc, 0, v0
	s_waitcnt vmcnt(0)
	buffer_inv sc1
	s_and_saveexec_b64 s[8:9], vcc
	s_cbranch_execz .LBB0_409
	s_bcnt1_i32_b64 s6, s[6:7]
	v_mov_b32_e32 v0, 0x2000
	v_mov_b32_e32 v1, s6
.LBB0_409:
	s_or_b64 exec, exec, s[8:9]
	s_waitcnt vmcnt(0)

.LBB0_479:
	s_or_b64 exec, exec, s[6:7]
	s_mov_b64 s[6:7], exec
	v_mbcnt_lo_u32_b32 v0, s6, 0
	v_mbcnt_hi_u32_b32 v0, s7, v0
	v_cmp_eq_u32_e32 vcc, 0, v0
	s_waitcnt vmcnt(0)
	buffer_inv sc1
	s_and_saveexec_b64 s[8:9], vcc
	s_cbranch_execz .LBB0_481
	s_bcnt1_i32_b64 s6, s[6:7]
	v_mov_b32_e32 v0, 0x2000
	v_mov_b32_e32 v1, s6
.LBB0_481:
	s_or_b64 exec, exec, s[8:9]
	s_waitcnt vmcnt(0)

.LBB0_552:
	s_or_b64 exec, exec, s[6:7]
	s_mov_b64 s[6:7], exec
	v_mbcnt_lo_u32_b32 v0, s6, 0
	v_mbcnt_hi_u32_b32 v0, s7, v0
	v_cmp_eq_u32_e32 vcc, 0, v0
	s_waitcnt vmcnt(0)
	buffer_inv sc1
	s_and_saveexec_b64 s[8:9], vcc
	s_cbranch_execz .LBB0_554
	s_bcnt1_i32_b64 s6, s[6:7]
	v_mov_b32_e32 v0, 0x2000
	v_mov_b32_e32 v1, s6
.LBB0_554:
	s_or_b64 exec, exec, s[8:9]
	s_waitcnt vmcnt(0)

.LBB0_629:
	s_or_b64 exec, exec, s[6:7]
	s_mov_b64 s[6:7], exec
	v_mbcnt_lo_u32_b32 v0, s6, 0
	v_mbcnt_hi_u32_b32 v0, s7, v0
	v_cmp_eq_u32_e32 vcc, 0, v0
	s_waitcnt vmcnt(0)
	buffer_inv sc1
	s_and_saveexec_b64 s[8:9], vcc
	s_cbranch_execz .LBB0_631
	s_bcnt1_i32_b64 s6, s[6:7]
	v_mov_b32_e32 v0, 0x2000
	v_mov_b32_e32 v1, s6
.LBB0_631:
	s_or_b64 exec, exec, s[8:9]
	s_waitcnt vmcnt(0)

.LBB0_691:
	s_or_b64 exec, exec, s[6:7]
	s_mov_b64 s[6:7], exec
	v_mbcnt_lo_u32_b32 v0, s6, 0
	v_mbcnt_hi_u32_b32 v0, s7, v0
	v_cmp_eq_u32_e32 vcc, 0, v0
	s_waitcnt vmcnt(0)
	buffer_inv sc1
	s_and_saveexec_b64 s[8:9], vcc
	s_cbranch_execz .LBB0_693
	s_bcnt1_i32_b64 s6, s[6:7]
	v_mov_b32_e32 v0, 0x2000
	v_mov_b32_e32 v1, s6
.LBB0_693:
	s_or_b64 exec, exec, s[8:9]
	s_waitcnt vmcnt(0)

.LBB0_773:
	s_or_b64 exec, exec, s[6:7]
	s_mov_b64 s[6:7], exec
	v_mbcnt_lo_u32_b32 v0, s6, 0
	v_mbcnt_hi_u32_b32 v0, s7, v0
	v_cmp_eq_u32_e32 vcc, 0, v0
	s_waitcnt vmcnt(0)
	buffer_inv sc1
	s_and_saveexec_b64 s[8:9], vcc
	s_cbranch_execz .LBB0_775
	s_bcnt1_i32_b64 s6, s[6:7]
	v_mov_b32_e32 v0, 0x2000
	v_mov_b32_e32 v1, s6
.LBB0_775:
	s_or_b64 exec, exec, s[8:9]
	s_waitcnt vmcnt(0)

.LBB0_840:
	s_or_b64 exec, exec, s[6:7]
	s_mov_b64 s[6:7], exec
	v_mbcnt_lo_u32_b32 v0, s6, 0
	v_mbcnt_hi_u32_b32 v0, s7, v0
	v_cmp_eq_u32_e32 vcc, 0, v0
	s_waitcnt vmcnt(0)
	buffer_inv sc1
	s_and_saveexec_b64 s[8:9], vcc
	s_cbranch_execz .LBB0_842
	s_bcnt1_i32_b64 s6, s[6:7]
	v_mov_b32_e32 v0, 0x2000
	v_mov_b32_e32 v1, s6
.LBB0_842:
	s_or_b64 exec, exec, s[8:9]
	s_waitcnt vmcnt(0)

.LBB0_1603:
	s_or_b64 exec, exec, s[6:7]
	s_mov_b64 s[6:7], exec
	v_mbcnt_lo_u32_b32 v0, s6, 0
	v_mbcnt_hi_u32_b32 v0, s7, v0
	v_cmp_eq_u32_e32 vcc, 0, v0
	s_waitcnt vmcnt(0)
	buffer_inv sc1
	s_and_saveexec_b64 s[8:9], vcc
	s_cbranch_execz .LBB0_1605
	s_bcnt1_i32_b64 s6, s[6:7]
	v_mov_b32_e32 v0, 0x2000
	v_mov_b32_e32 v1, s6
.LBB0_1605:
	s_or_b64 exec, exec, s[8:9]
	s_waitcnt vmcnt(0)

.LBB0_1680:
	s_or_b64 exec, exec, s[6:7]
	s_mov_b64 s[6:7], exec
	v_mbcnt_lo_u32_b32 v0, s6, 0
	v_mbcnt_hi_u32_b32 v0, s7, v0
	v_cmp_eq_u32_e32 vcc, 0, v0
	s_waitcnt vmcnt(0)
	buffer_inv sc1
	s_and_saveexec_b64 s[8:9], vcc
	s_cbranch_execz .LBB0_1682
	s_bcnt1_i32_b64 s6, s[6:7]
	v_mov_b32_e32 v0, 0x2000
	v_mov_b32_e32 v1, s6
.LBB0_1682:
	s_or_b64 exec, exec, s[8:9]
	s_waitcnt vmcnt(0)

.LBB0_1765:
	s_or_b64 exec, exec, s[6:7]
	s_mov_b64 s[6:7], exec
	v_mbcnt_lo_u32_b32 v0, s6, 0
	v_mbcnt_hi_u32_b32 v0, s7, v0
	v_cmp_eq_u32_e32 vcc, 0, v0
	s_waitcnt vmcnt(0)
	buffer_inv sc1
	s_and_saveexec_b64 s[8:9], vcc
	s_cbranch_execz .LBB0_1767
	s_bcnt1_i32_b64 s6, s[6:7]
	v_mov_b32_e32 v0, 0x2000
	v_mov_b32_e32 v1, s6
.LBB0_1767:
	s_or_b64 exec, exec, s[8:9]
	s_waitcnt vmcnt(0)

.LBB0_1831:
	s_or_b64 exec, exec, s[6:7]
	s_mov_b64 s[6:7], exec
	v_mbcnt_lo_u32_b32 v0, s6, 0
	v_mbcnt_hi_u32_b32 v0, s7, v0
	v_cmp_eq_u32_e32 vcc, 0, v0
	s_waitcnt vmcnt(0)
	buffer_inv sc1
	s_and_saveexec_b64 s[8:9], vcc
	s_cbranch_execz .LBB0_1833
	s_bcnt1_i32_b64 s6, s[6:7]
	v_mov_b32_e32 v0, 0x2000
	v_mov_b32_e32 v1, s6
.LBB0_1833:
	s_or_b64 exec, exec, s[8:9]
	s_waitcnt vmcnt(0)

.LBB0_1906:
	s_or_b64 exec, exec, s[6:7]
	s_mov_b64 s[6:7], exec
	v_mbcnt_lo_u32_b32 v0, s6, 0
	v_mbcnt_hi_u32_b32 v0, s7, v0
	v_cmp_eq_u32_e32 vcc, 0, v0
	s_waitcnt vmcnt(0)
	buffer_inv sc1
	s_and_saveexec_b64 s[8:9], vcc
	s_cbranch_execz .LBB0_1908
	s_bcnt1_i32_b64 s6, s[6:7]
	v_mov_b32_e32 v0, 0x2000
	v_mov_b32_e32 v1, s6
.LBB0_1908:
	s_or_b64 exec, exec, s[8:9]
	s_waitcnt vmcnt(0)

.LBB0_1981:
	s_or_b64 exec, exec, s[6:7]
	s_mov_b64 s[6:7], exec
	v_mbcnt_lo_u32_b32 v0, s6, 0
	v_mbcnt_hi_u32_b32 v0, s7, v0
	v_cmp_eq_u32_e32 vcc, 0, v0
	s_waitcnt vmcnt(0)
	buffer_inv sc1
	s_and_saveexec_b64 s[8:9], vcc
	s_cbranch_execz .LBB0_1983
	s_bcnt1_i32_b64 s6, s[6:7]
	v_mov_b32_e32 v0, 0x2000
	v_mov_b32_e32 v1, s6
.LBB0_1983:
	s_or_b64 exec, exec, s[8:9]
	s_waitcnt vmcnt(0)

.LBB0_2065:
	s_or_b64 exec, exec, s[6:7]
	s_mov_b64 s[6:7], exec
	v_mbcnt_lo_u32_b32 v0, s6, 0
	v_mbcnt_hi_u32_b32 v0, s7, v0
	v_cmp_eq_u32_e32 vcc, 0, v0
	s_waitcnt vmcnt(0)
	buffer_inv sc1
	s_and_saveexec_b64 s[8:9], vcc
	s_cbranch_execz .LBB0_2067
	s_bcnt1_i32_b64 s6, s[6:7]
	v_mov_b32_e32 v0, 0x2000
	v_mov_b32_e32 v1, s6
.LBB0_2067:
	s_or_b64 exec, exec, s[8:9]
	s_waitcnt vmcnt(0)
